# attention: s_setprio 1 during MFMA (PV/QK) intervals of both ping-pong halves, 0 during softmax intervals
# baseline (speedup 1.0000x reference)
.LBB0_370:
	s_waitcnt vmcnt(2)
	s_cmp_lt_u32 s82, s63
	s_waitcnt lgkmcnt(0)
	s_setprio 0
	s_barrier
	s_cselect_b64 s[8:9], -1, 0
	s_cmp_ge_u32 s82, s63
	s_cselect_b64 s[24:25], -1, 0
	s_and_b64 vcc, exec, s[24:25]
	s_cbranch_vccnz .LBB0_372
	v_mov_b32_e32 v2, v197
	s_add_i32 s6, s83, 0x4000
	v_ashrrev_i32_e32 v4, 4, v2
	v_lshlrev_b32_e32 v5, 12, v4
	v_add_u32_e32 v6, s89, v4
	v_add_u32_e32 v4, s93, v4
	v_xor_b32_e32 v6, v6, v2
	v_xor_b32_e32 v2, v4, v2
	v_lshlrev_b32_e32 v6, 4, v6
	v_lshlrev_b32_e32 v2, 4, v2
	s_and_b32 s6, s6, 0x4000
	v_and_or_b32 v6, v6, s51, v5
	v_and_or_b32 v2, v2, s51, v5
	s_add_i32 s6, s6, s77
	s_mov_b32 s7, m0
	s_mov_b32 m0, s6
	s_nop 0
	global_load_lds_dwordx4 v6, s[18:19]
	s_mov_b32 m0, s7
	v_add_u32_e32 v2, 0x4000, v2
	s_addk_i32 s6, 0x400
	s_mov_b32 s7, m0
	s_mov_b32 m0, s6
	s_nop 0
	global_load_lds_dwordx4 v2, s[18:19]
	s_mov_b32 m0, s7

.LBB0_384:
	s_waitcnt lgkmcnt(0)
	s_barrier
	s_setprio 1
	v_cndmask_b32_e64 v2, 0, 1, s[36:37]
	v_cmp_ne_u32_e64 s[10:11], 1, v2
	s_andn2_b64 vcc, exec, s[36:37]
	s_cbranch_vccnz .LBB0_387
	s_add_i32 s6, s82, -2
	s_cmp_gt_i32 s6, s62
	s_cbranch_scc1 .LBB0_387
	s_add_i32 s6, s83, 0xffffc000
	s_and_b32 s6, s6, 0x4000
	v_add_u32_e32 v2, s6, v213
	ds_read_b64_tr_b16 v[4:5], v2 offset:32768
	ds_read_b64_tr_b16 v[6:7], v2 offset:33280
	ds_read_b64_tr_b16 v[8:9], v2 offset:33792
	ds_read_b64_tr_b16 v[10:11], v2 offset:34304
	ds_read_b64_tr_b16 v[12:13], v2 offset:40960
	ds_read_b64_tr_b16 v[14:15], v2 offset:41472
	ds_read_b64_tr_b16 v[198:199], v2 offset:41984
	ds_read_b64_tr_b16 v[200:201], v2 offset:42496
	ds_read_b64_tr_b16 v[222:223], v2 offset:36864
	ds_read_b64_tr_b16 v[224:225], v2 offset:37376
	ds_read_b64_tr_b16 v[226:227], v2 offset:34816
	ds_read_b64_tr_b16 v[228:229], v2 offset:35328
	ds_read_b64_tr_b16 v[230:231], v2 offset:37888
	ds_read_b64_tr_b16 v[232:233], v2 offset:38400
	ds_read_b64_tr_b16 v[234:235], v2 offset:38912
	ds_read_b64_tr_b16 v[236:237], v2 offset:39424
	ds_read_b64_tr_b16 v[238:239], v2 offset:45056
	ds_read_b64_tr_b16 v[240:241], v2 offset:45568
	ds_read_b64_tr_b16 v[242:243], v2 offset:43008
	ds_read_b64_tr_b16 v[244:245], v2 offset:43520
	ds_read_b64_tr_b16 v[246:247], v2 offset:46080
	ds_read_b64_tr_b16 v[248:249], v2 offset:46592
	ds_read_b64_tr_b16 v[250:251], v2 offset:47104
	ds_read_b64_tr_b16 v[252:253], v2 offset:47616
	s_waitcnt lgkmcnt(14)
	v_mfma_f32_32x32x16_bf16 v[130:145], v[4:7], v[182:185], v[130:145]
	v_mfma_f32_32x32x16_bf16 v[98:113], v[222:225], v[182:185], v[98:113]
	v_mfma_f32_32x32x16_bf16 v[66:81], v[12:15], v[182:185], v[66:81]
	s_waitcnt lgkmcnt(6)
	v_mfma_f32_32x32x16_bf16 v[34:49], v[238:241], v[182:185], v[34:49]
	ds_read_b64_tr_b16 v[4:5], v2 offset:35840
	ds_read_b64_tr_b16 v[6:7], v2 offset:36352
	ds_read_b64_tr_b16 v[12:13], v2 offset:39936
	ds_read_b64_tr_b16 v[14:15], v2 offset:40448
	ds_read_b64_tr_b16 v[222:223], v2 offset:44032
	ds_read_b64_tr_b16 v[224:225], v2 offset:44544
	ds_read_b64_tr_b16 v[238:239], v2 offset:48128
	ds_read_b64_tr_b16 v[240:241], v2 offset:48640
	v_mfma_f32_32x32x16_bf16 v[130:145], v[8:11], v[186:189], v[130:145]
	v_mfma_f32_32x32x16_bf16 v[98:113], v[230:233], v[186:189], v[98:113]
	v_mfma_f32_32x32x16_bf16 v[66:81], v[198:201], v[186:189], v[66:81]
	s_waitcnt lgkmcnt(10)
	v_mfma_f32_32x32x16_bf16 v[34:49], v[246:249], v[186:189], v[34:49]
	v_mfma_f32_32x32x16_bf16 v[130:145], v[226:229], v[178:181], v[130:145]
	v_mfma_f32_32x32x16_bf16 v[98:113], v[234:237], v[178:181], v[98:113]
	v_mfma_f32_32x32x16_bf16 v[66:81], v[242:245], v[178:181], v[66:81]
	s_waitcnt lgkmcnt(8)
	v_mfma_f32_32x32x16_bf16 v[34:49], v[250:253], v[178:181], v[34:49]
	s_waitcnt lgkmcnt(6)
	v_mfma_f32_32x32x16_bf16 v[130:145], v[4:7], v[190:193], v[130:145]
	s_waitcnt lgkmcnt(4)
	v_mfma_f32_32x32x16_bf16 v[98:113], v[12:15], v[190:193], v[98:113]
	s_waitcnt lgkmcnt(2)
	v_mfma_f32_32x32x16_bf16 v[66:81], v[222:225], v[190:193], v[66:81]
	s_waitcnt lgkmcnt(0)
	v_mfma_f32_32x32x16_bf16 v[34:49], v[238:241], v[190:193], v[34:49]

.LBB0_391:
	s_waitcnt lgkmcnt(0)
	s_setprio 0
	s_barrier
	s_andn2_b64 vcc, exec, s[8:9]
	s_cbranch_vccnz .LBB0_393
	v_mov_b32_e32 v2, v197
	s_lshl_b32 s6, s82, 14
	s_and_b32 s6, s6, 0x4000
	v_lshlrev_b32_e32 v4, 10, v2
	v_lshlrev_b32_e32 v2, 4, v2
	s_add_i32 s6, s6, 0
	v_and_b32_e32 v2, 48, v2
	s_add_i32 s6, s6, 0x8000
	v_and_or_b32 v2, v4, s1, v2
	s_add_i32 s7, s6, s52
	s_mov_b32 s8, m0
	s_mov_b32 m0, s7
	s_nop 0
	global_load_lds_dwordx4 v2, s[20:21]
	s_mov_b32 m0, s8
	s_add_i32 s6, s6, s94
	s_mov_b32 s7, m0
	s_mov_b32 m0, s6
	s_nop 0
	global_load_lds_dwordx4 v2, s[22:23]
	s_mov_b32 m0, s7

.LBB0_404:
	s_waitcnt lgkmcnt(0)
	s_barrier
	s_setprio 1
	s_and_b64 vcc, exec, s[8:9]
	s_cbranch_vccnz .LBB0_369
	s_and_b32 s6, s83, 0x4000
	s_add_i32 s6, s6, 0
	v_add_u32_e32 v2, s6, v205
	ds_read_b64_tr_b16 v[4:5], v2 offset:32768
	ds_read_b64_tr_b16 v[6:7], v2 offset:33280
	ds_read_b64_tr_b16 v[8:9], v2 offset:33792
	ds_read_b64_tr_b16 v[10:11], v2 offset:34304
	ds_read_b64_tr_b16 v[12:13], v2 offset:40960
	ds_read_b64_tr_b16 v[14:15], v2 offset:41472
	ds_read_b64_tr_b16 v[146:147], v2 offset:41984
	ds_read_b64_tr_b16 v[148:149], v2 offset:42496
	ds_read_b64_tr_b16 v[150:151], v2 offset:36864
	ds_read_b64_tr_b16 v[152:153], v2 offset:37376
	ds_read_b64_tr_b16 v[154:155], v2 offset:34816
	ds_read_b64_tr_b16 v[156:157], v2 offset:35328
	ds_read_b64_tr_b16 v[158:159], v2 offset:37888
	ds_read_b64_tr_b16 v[160:161], v2 offset:38400
	ds_read_b64_tr_b16 v[162:163], v2 offset:38912
	ds_read_b64_tr_b16 v[164:165], v2 offset:39424
	ds_read_b64_tr_b16 v[166:167], v2 offset:45056
	ds_read_b64_tr_b16 v[168:169], v2 offset:45568
	ds_read_b64_tr_b16 v[170:171], v2 offset:43008
	ds_read_b64_tr_b16 v[172:173], v2 offset:43520
	ds_read_b64_tr_b16 v[174:175], v2 offset:46080
	ds_read_b64_tr_b16 v[176:177], v2 offset:46592
	ds_read_b64_tr_b16 v[198:199], v2 offset:47104
	ds_read_b64_tr_b16 v[200:201], v2 offset:47616
	s_waitcnt lgkmcnt(14)
	v_mfma_f32_32x32x16_bf16 v[114:129], v[4:7], v[182:185], v[114:129]
	v_mfma_f32_32x32x16_bf16 v[82:97], v[150:153], v[182:185], v[82:97]
	v_mfma_f32_32x32x16_bf16 v[50:65], v[12:15], v[182:185], v[50:65]
	s_waitcnt lgkmcnt(6)
	v_mfma_f32_32x32x16_bf16 v[18:33], v[166:169], v[182:185], v[18:33]
	ds_read_b64_tr_b16 v[4:5], v2 offset:35840
	ds_read_b64_tr_b16 v[6:7], v2 offset:36352
	ds_read_b64_tr_b16 v[12:13], v2 offset:39936
	ds_read_b64_tr_b16 v[14:15], v2 offset:40448
	ds_read_b64_tr_b16 v[150:151], v2 offset:44032
	ds_read_b64_tr_b16 v[152:153], v2 offset:44544
	ds_read_b64_tr_b16 v[166:167], v2 offset:48128
	ds_read_b64_tr_b16 v[168:169], v2 offset:48640
	v_mfma_f32_32x32x16_bf16 v[114:129], v[8:11], v[186:189], v[114:129]
	v_mfma_f32_32x32x16_bf16 v[82:97], v[158:161], v[186:189], v[82:97]
	v_mfma_f32_32x32x16_bf16 v[50:65], v[146:149], v[186:189], v[50:65]
	s_waitcnt lgkmcnt(10)
	v_mfma_f32_32x32x16_bf16 v[18:33], v[174:177], v[186:189], v[18:33]
	v_mfma_f32_32x32x16_bf16 v[114:129], v[154:157], v[178:181], v[114:129]
	v_mfma_f32_32x32x16_bf16 v[82:97], v[162:165], v[178:181], v[82:97]
	v_mfma_f32_32x32x16_bf16 v[50:65], v[170:173], v[178:181], v[50:65]
	s_waitcnt lgkmcnt(8)
	v_mfma_f32_32x32x16_bf16 v[18:33], v[198:201], v[178:181], v[18:33]
	s_waitcnt lgkmcnt(6)
	v_mfma_f32_32x32x16_bf16 v[114:129], v[4:7], v[190:193], v[114:129]
	s_waitcnt lgkmcnt(4)
	v_mfma_f32_32x32x16_bf16 v[82:97], v[12:15], v[190:193], v[82:97]
	s_waitcnt lgkmcnt(2)
	v_mfma_f32_32x32x16_bf16 v[50:65], v[150:153], v[190:193], v[50:65]
	s_waitcnt lgkmcnt(0)
	v_mfma_f32_32x32x16_bf16 v[18:33], v[166:169], v[190:193], v[18:33]
	v_add_u32_e32 v2, s6, v206
	v_add_u32_e32 v16, s6, v207
	ds_read_b128 v[4:7], v2 offset:8192
	ds_read_b128 v[8:11], v16
	ds_read_b128 v[12:15], v203 offset:4096
	ds_read_b128 v[198:201], v203 offset:5120
	v_add_u32_e32 v17, s6, v210
	ds_read_b128 v[222:225], v16 offset:8192
	ds_read_b128 v[226:229], v17
	ds_read_b128 v[230:233], v17 offset:8192
	ds_read_b128 v[234:237], v2
	ds_read_b128 v[238:241], v203 offset:6144
	v_xor_b32_e32 v146, 0x80000000, v220
	v_mov_b32_e32 v147, v146
	v_mov_b32_e32 v148, v146
	v_mov_b32_e32 v149, v146
	v_mov_b32_e32 v150, v146
	v_mov_b32_e32 v151, v146
	v_mov_b32_e32 v152, v146
	v_mov_b32_e32 v153, v146
	v_mov_b32_e32 v154, v146
	v_mov_b32_e32 v155, v146
	v_mov_b32_e32 v156, v146
	v_mov_b32_e32 v157, v146
	v_mov_b32_e32 v158, v146
	v_mov_b32_e32 v159, v146
	v_mov_b32_e32 v160, v146
	v_mov_b32_e32 v161, v146
	s_waitcnt lgkmcnt(1)
	s_nop 0
	v_mfma_f32_32x32x16_bf16 v[162:177], v[234:237], v[12:15], v[146:161]
	v_mfma_f32_32x32x16_bf16 v[146:161], v[4:7], v[12:15], v[146:161]
	v_add_u32_e32 v2, s6, v211
	ds_read_b128 v[4:7], v2 offset:8192
	ds_read_b128 v[12:15], v2
	ds_read_b128 v[234:237], v203 offset:7168
	v_mfma_f32_32x32x16_bf16 v[162:177], v[8:11], v[198:201], v[162:177]
	v_mfma_f32_32x32x16_bf16 v[146:161], v[222:225], v[198:201], v[146:161]
	s_waitcnt lgkmcnt(3)
	v_mfma_f32_32x32x16_bf16 v[162:177], v[226:229], v[238:241], v[162:177]
	v_mfma_f32_32x32x16_bf16 v[146:161], v[230:233], v[238:241], v[146:161]
	s_waitcnt lgkmcnt(0)
	v_mfma_f32_32x32x16_bf16 v[162:177], v[12:15], v[234:237], v[162:177]
	v_mfma_f32_32x32x16_bf16 v[146:161], v[4:7], v[234:237], v[146:161]
	s_branch .LBB0_369

.LBB0_410:
	s_setprio 0
	s_waitcnt vmcnt(0)
	s_waitcnt lgkmcnt(0)
	s_barrier
	v_cndmask_b32_e64 v2, 0, 1, s[58:59]
	v_cmp_ne_u32_e64 s[8:9], 1, v2
	s_andn2_b64 vcc, exec, s[58:59]
	s_cbranch_vccnz .LBB0_416
	v_readlane_b32 s6, v255, 32
	v_readlane_b32 s7, v255, 33
	s_andn2_b64 vcc, exec, s[6:7]
	v_mov_b32_e32 v219, v221
	s_cbranch_vccnz .LBB0_413
	v_or_b32_e32 v2, s97, v217
	v_sub_u32_e32 v2, 0xc0, v2
	s_add_i32 s6, 0, 0x20000
	v_lshlrev_b32_e32 v2, 2, v2
	v_lshlrev_b32_e32 v4, 2, v196
	v_add3_u32 v2, s6, v2, v4
	ds_read2_b32 v[4:5], v2 offset0:184 offset1:185
	ds_read2_b32 v[6:7], v2 offset0:186 offset1:187
	ds_read2_b32 v[8:9], v2 offset0:192 offset1:193
	ds_read2_b32 v[10:11], v2 offset0:194 offset1:195
	ds_read2_b32 v[12:13], v2 offset0:200 offset1:201
	ds_read2_b32 v[14:15], v2 offset0:202 offset1:203
	ds_read2_b32 v[16:17], v2 offset0:208 offset1:209
	ds_read2_b32 v[178:179], v2 offset0:210 offset1:211
	ds_read2_b32 v[180:181], v2 offset0:216 offset1:217
	ds_read2_b32 v[182:183], v2 offset0:218 offset1:219
	ds_read2_b32 v[184:185], v2 offset0:224 offset1:225
	ds_read2_b32 v[186:187], v2 offset0:226 offset1:227
	s_waitcnt lgkmcnt(4)
	v_add_f32_e32 v176, v176, v178
	v_add_f32_e32 v177, v177, v179
	v_add_f32_e32 v174, v174, v16
	v_add_f32_e32 v175, v175, v17
	v_add_f32_e32 v172, v172, v14
	v_add_f32_e32 v173, v173, v15
	v_add_f32_e32 v170, v170, v12
	v_add_f32_e32 v171, v171, v13
	ds_read2_b32 v[12:13], v2 offset0:232 offset1:233
	ds_read2_b32 v[14:15], v2 offset0:234 offset1:235
	ds_read2_b32 v[16:17], v2 offset0:240 offset1:241
	ds_read2_b32 v[178:179], v2 offset0:242 offset1:243
	v_add_f32_e32 v168, v168, v10
	v_add_f32_e32 v169, v169, v11
	v_add_f32_e32 v166, v166, v8
	v_add_f32_e32 v167, v167, v9
	v_add_f32_e32 v164, v164, v6
	v_add_f32_e32 v165, v165, v7
	v_add_f32_e32 v162, v162, v4
	v_add_f32_e32 v163, v163, v5
	s_waitcnt lgkmcnt(0)
	v_add_f32_e32 v160, v160, v178
	v_add_f32_e32 v161, v161, v179
	v_add_f32_e32 v158, v158, v16
	v_add_f32_e32 v159, v159, v17
	v_add_f32_e32 v156, v156, v14
	v_add_f32_e32 v157, v157, v15
	v_add_f32_e32 v154, v154, v12
	v_add_f32_e32 v155, v155, v13
	v_add_f32_e32 v152, v152, v186
	v_add_f32_e32 v153, v153, v187
	v_add_f32_e32 v150, v150, v184
	v_add_f32_e32 v151, v151, v185
	v_add_f32_e32 v148, v148, v182
	v_add_f32_e32 v149, v149, v183
	v_add_f32_e32 v146, v146, v180
	v_add_f32_e32 v147, v147, v181

.LBB0_425:
	s_waitcnt vmcnt(2)
	s_cmp_lt_u32 s39, s63
	s_waitcnt lgkmcnt(0)
	s_barrier
	s_setprio 1
	s_cselect_b64 s[20:21], -1, 0
	s_cmp_ge_u32 s39, s63
	s_cselect_b64 s[22:23], -1, 0
	s_and_b64 vcc, exec, s[22:23]
	s_cbranch_vccnz .LBB0_427
	v_mov_b32_e32 v2, v197
	s_add_i32 s6, s37, 0x4000
	v_ashrrev_i32_e32 v4, 4, v2
	v_lshlrev_b32_e32 v5, 12, v4
	v_add_u32_e32 v6, s89, v4
	v_add_u32_e32 v4, s93, v4
	v_xor_b32_e32 v6, v6, v2
	v_xor_b32_e32 v2, v4, v2
	v_lshlrev_b32_e32 v6, 4, v6
	v_lshlrev_b32_e32 v2, 4, v2
	s_and_b32 s6, s6, 0x4000
	v_and_or_b32 v6, v6, s51, v5
	v_and_or_b32 v2, v2, s51, v5
	s_add_i32 s6, s6, s77
	s_mov_b32 s7, m0
	s_mov_b32 m0, s6
	s_nop 0
	global_load_lds_dwordx4 v6, s[16:17]
	s_mov_b32 m0, s7
	v_add_u32_e32 v2, 0x4000, v2
	s_addk_i32 s6, 0x400
	s_mov_b32 s7, m0
	s_mov_b32 m0, s6
	s_nop 0
	global_load_lds_dwordx4 v2, s[16:17]
	s_mov_b32 m0, s7

.LBB0_432:
	s_waitcnt lgkmcnt(0)
	s_setprio 0
	s_barrier
	v_cndmask_b32_e64 v2, 0, 1, s[10:11]
	v_cmp_ne_u32_e64 s[8:9], 1, v2
	s_andn2_b64 vcc, exec, s[10:11]
	s_cbranch_vccnz .LBB0_443
	s_cmp_le_i32 s65, s64
	s_cbranch_scc1 .LBB0_435
	v_add_u32_e32 v2, s38, v216
	v_add_u32_e32 v4, 0x206e0, v2
	v_add_u32_e32 v6, 0x20760, v2
	ds_read2_b32 v[4:5], v4 offset1:1
	ds_read2_b32 v[6:7], v6 offset1:1
	v_add_u32_e32 v8, 0x206e8, v2
	v_add_u32_e32 v10, 0x20768, v2
	v_add_u32_e32 v12, 0x20700, v2
	v_add_u32_e32 v14, 0x20780, v2
	v_add_u32_e32 v16, 0x20708, v2
	v_add_u32_e32 v178, 0x20788, v2
	v_add_u32_e32 v180, 0x20720, v2
	v_add_u32_e32 v182, 0x207a0, v2
	v_add_u32_e32 v184, 0x20728, v2
	v_add_u32_e32 v186, 0x207a8, v2
	v_add_u32_e32 v188, 0x20740, v2
	v_add_u32_e32 v190, 0x207c0, v2
	v_add_u32_e32 v192, 0x20748, v2
	v_add_u32_e32 v2, 0x207c8, v2
	ds_read2_b32 v[8:9], v8 offset1:1
	ds_read2_b32 v[10:11], v10 offset1:1
	ds_read2_b32 v[12:13], v12 offset1:1
	ds_read2_b32 v[14:15], v14 offset1:1
	ds_read2_b32 v[16:17], v16 offset1:1
	ds_read2_b32 v[178:179], v178 offset1:1
	ds_read2_b32 v[180:181], v180 offset1:1
	ds_read2_b32 v[182:183], v182 offset1:1
	ds_read2_b32 v[184:185], v184 offset1:1
	ds_read2_b32 v[186:187], v186 offset1:1
	ds_read2_b32 v[188:189], v188 offset1:1
	ds_read2_b32 v[190:191], v190 offset1:1
	ds_read2_b32 v[192:193], v192 offset1:1
	s_waitcnt lgkmcnt(14)
	v_add_f32_e32 v162, v162, v4
	v_add_f32_e32 v163, v163, v5
	ds_read2_b32 v[4:5], v2 offset1:1
	s_waitcnt lgkmcnt(3)
	v_add_f32_e32 v174, v174, v188
	v_add_f32_e32 v175, v175, v189
	v_add_f32_e32 v172, v172, v184
	v_add_f32_e32 v173, v173, v185
	s_waitcnt lgkmcnt(1)
	v_add_f32_e32 v176, v176, v192
	v_add_f32_e32 v177, v177, v193
	v_add_f32_e32 v170, v170, v180
	v_add_f32_e32 v171, v171, v181
	v_add_f32_e32 v168, v168, v16
	v_add_f32_e32 v169, v169, v17
	v_add_f32_e32 v166, v166, v12
	v_add_f32_e32 v167, v167, v13
	v_add_f32_e32 v164, v164, v8
	v_add_f32_e32 v165, v165, v9
	s_waitcnt lgkmcnt(0)
	v_add_f32_e32 v160, v160, v4
	v_add_f32_e32 v161, v161, v5
	v_add_f32_e32 v158, v158, v190
	v_add_f32_e32 v159, v159, v191
	v_add_f32_e32 v156, v156, v186
	v_add_f32_e32 v157, v157, v187
	v_add_f32_e32 v154, v154, v182
	v_add_f32_e32 v155, v155, v183
	v_add_f32_e32 v152, v152, v178
	v_add_f32_e32 v153, v153, v179
	v_add_f32_e32 v150, v150, v14
	v_add_f32_e32 v151, v151, v15
	v_add_f32_e32 v148, v148, v10
	v_add_f32_e32 v149, v149, v11
	v_add_f32_e32 v146, v146, v6
	v_add_f32_e32 v147, v147, v7

.LBB0_447:
	s_waitcnt lgkmcnt(0)
	s_barrier
	s_setprio 1
	s_andn2_b64 vcc, exec, s[20:21]
	s_cbranch_vccnz .LBB0_449
	v_mov_b32_e32 v2, v197
	s_lshl_b32 s6, s39, 14
	s_and_b32 s6, s6, 0x4000
	v_lshlrev_b32_e32 v4, 10, v2
	v_lshlrev_b32_e32 v2, 4, v2
	s_add_i32 s6, s6, 0
	v_and_b32_e32 v2, 48, v2
	s_add_i32 s6, s6, 0x8000
	v_and_or_b32 v2, v4, s1, v2
	s_add_i32 s7, s6, s52
	s_mov_b32 s10, m0
	s_mov_b32 m0, s7
	s_nop 0
	global_load_lds_dwordx4 v2, s[14:15]
	s_mov_b32 m0, s10
	s_add_i32 s6, s6, s94
	s_mov_b32 s7, m0
	s_mov_b32 m0, s6
	s_nop 0
	global_load_lds_dwordx4 v2, s[12:13]
	s_mov_b32 m0, s7

.LBB0_451:
	s_waitcnt lgkmcnt(0)
	s_setprio 0
	s_barrier
	s_and_b64 vcc, exec, s[8:9]
	s_cbranch_vccnz .LBB0_424
	s_cmp_le_i32 s65, s64
	s_cbranch_scc1 .LBB0_454
	v_add_u32_e32 v2, s38, v216
	v_add_u32_e32 v4, 0x206e0, v2
	v_add_u32_e32 v6, 0x20760, v2
	ds_read2_b32 v[4:5], v4 offset1:1
	ds_read2_b32 v[6:7], v6 offset1:1
	v_add_u32_e32 v8, 0x206e8, v2
	v_add_u32_e32 v10, 0x20768, v2
	v_add_u32_e32 v12, 0x20700, v2
	v_add_u32_e32 v14, 0x20780, v2
	v_add_u32_e32 v16, 0x20708, v2
	v_add_u32_e32 v178, 0x20788, v2
	v_add_u32_e32 v180, 0x20720, v2
	v_add_u32_e32 v182, 0x207a0, v2
	v_add_u32_e32 v184, 0x20728, v2
	v_add_u32_e32 v186, 0x207a8, v2
	v_add_u32_e32 v188, 0x20740, v2
	v_add_u32_e32 v190, 0x207c0, v2
	v_add_u32_e32 v192, 0x20748, v2
	v_add_u32_e32 v2, 0x207c8, v2
	ds_read2_b32 v[8:9], v8 offset1:1
	ds_read2_b32 v[10:11], v10 offset1:1
	ds_read2_b32 v[12:13], v12 offset1:1
	ds_read2_b32 v[14:15], v14 offset1:1
	ds_read2_b32 v[16:17], v16 offset1:1
	ds_read2_b32 v[178:179], v178 offset1:1
	ds_read2_b32 v[180:181], v180 offset1:1
	ds_read2_b32 v[182:183], v182 offset1:1
	ds_read2_b32 v[184:185], v184 offset1:1
	ds_read2_b32 v[186:187], v186 offset1:1
	ds_read2_b32 v[188:189], v188 offset1:1
	ds_read2_b32 v[190:191], v190 offset1:1
	ds_read2_b32 v[192:193], v192 offset1:1
	s_waitcnt lgkmcnt(14)
	v_add_f32_e32 v162, v162, v4
	v_add_f32_e32 v163, v163, v5
	ds_read2_b32 v[4:5], v2 offset1:1
	s_waitcnt lgkmcnt(3)
	v_add_f32_e32 v174, v174, v188
	v_add_f32_e32 v175, v175, v189
	v_add_f32_e32 v172, v172, v184
	v_add_f32_e32 v173, v173, v185
	s_waitcnt lgkmcnt(1)
	v_add_f32_e32 v176, v176, v192
	v_add_f32_e32 v177, v177, v193
	v_add_f32_e32 v170, v170, v180
	v_add_f32_e32 v171, v171, v181
	v_add_f32_e32 v168, v168, v16
	v_add_f32_e32 v169, v169, v17
	v_add_f32_e32 v166, v166, v12
	v_add_f32_e32 v167, v167, v13
	v_add_f32_e32 v164, v164, v8
	v_add_f32_e32 v165, v165, v9
	s_waitcnt lgkmcnt(0)
	v_add_f32_e32 v160, v160, v4
	v_add_f32_e32 v161, v161, v5
	v_add_f32_e32 v158, v158, v190
	v_add_f32_e32 v159, v159, v191
	v_add_f32_e32 v156, v156, v186
	v_add_f32_e32 v157, v157, v187
	v_add_f32_e32 v154, v154, v182
	v_add_f32_e32 v155, v155, v183
	v_add_f32_e32 v152, v152, v178
	v_add_f32_e32 v153, v153, v179
	v_add_f32_e32 v150, v150, v14
	v_add_f32_e32 v151, v151, v15
	v_add_f32_e32 v148, v148, v10
	v_add_f32_e32 v149, v149, v11
	v_add_f32_e32 v146, v146, v6
	v_add_f32_e32 v147, v147, v7
